# speedup vs baseline: 1.0763x; 1.0290x over previous
.LBB2_4:
	s_or_b64 exec, exec, s[4:5]
	v_mov_b32_e32 v17, 0
	s_waitcnt lgkmcnt(0)
	s_barrier
	ds_read_b32 v2, v17 offset:32776
	s_load_dwordx4 s[4:7], s[0:1], 0x8
	v_lshrrev_b32_e32 v1, 6, v0
	v_and_b32_e32 v28, 63, v0
	s_movk_i32 s3, 0x1000
	s_waitcnt lgkmcnt(0)
	v_readfirstlane_b32 s0, v2
	s_and_b32 s24, s0, 31
	v_lshlrev_b32_e32 v2, 16, v1
	v_lshl_or_b32 v2, s24, 18, v2
	v_lshl_or_b32 v16, v28, 5, v2
	v_lshl_add_u64 v[2:3], s[14:15], 0, v[16:17]
	v_mov_b32_e32 v115, 0
	v_lshlrev_b32_e32 v110, 11, v1
	v_add_u32_e32 v111, 1, v1
	v_and_b32_e32 v111, 3, v111
	v_lshlrev_b32_e32 v111, 11, v111
	v_add_u32_e32 v112, 2, v1
	v_and_b32_e32 v112, 3, v112
	v_lshlrev_b32_e32 v112, 11, v112
	v_add_u32_e32 v113, 3, v1
	v_and_b32_e32 v113, 3, v113
	v_lshlrev_b32_e32 v113, 11, v113
	v_mov_b32_e32 v114, v110
	v_lshl_add_u64 v[116:117], v[2:3], 0, v[114:115]
	global_load_dwordx4 a[0:3], v[116:117], off
	global_load_dwordx4 a[4:7], v[116:117], off offset:16
	v_add_u32_e32 v114, 0x2000, v110
	v_lshl_add_u64 v[116:117], v[2:3], 0, v[114:115]
	global_load_dwordx4 a[8:11], v[116:117], off
	global_load_dwordx4 a[12:15], v[116:117], off offset:16
	v_add_u32_e32 v114, 0x4000, v110
	v_lshl_add_u64 v[116:117], v[2:3], 0, v[114:115]
	global_load_dwordx4 a[16:19], v[116:117], off
	global_load_dwordx4 a[20:23], v[116:117], off offset:16
	v_add_u32_e32 v114, 0x6000, v110
	v_lshl_add_u64 v[116:117], v[2:3], 0, v[114:115]
	global_load_dwordx4 a[24:27], v[116:117], off
	global_load_dwordx4 a[28:31], v[116:117], off offset:16
	v_mov_b32_e32 v114, v111
	v_lshl_add_u64 v[116:117], v[2:3], 0, v[114:115]
	global_load_dwordx4 a[32:35], v[116:117], off
	global_load_dwordx4 a[36:39], v[116:117], off offset:16
	v_add_u32_e32 v114, 0x2000, v111
	v_lshl_add_u64 v[116:117], v[2:3], 0, v[114:115]
	global_load_dwordx4 a[40:43], v[116:117], off
	global_load_dwordx4 a[44:47], v[116:117], off offset:16
	v_add_u32_e32 v114, 0x4000, v111
	v_lshl_add_u64 v[116:117], v[2:3], 0, v[114:115]
	global_load_dwordx4 a[48:51], v[116:117], off
	global_load_dwordx4 a[52:55], v[116:117], off offset:16
	v_add_u32_e32 v114, 0x6000, v111
	v_lshl_add_u64 v[116:117], v[2:3], 0, v[114:115]
	global_load_dwordx4 a[56:59], v[116:117], off
	global_load_dwordx4 a[60:63], v[116:117], off offset:16
	v_mov_b32_e32 v114, v112
	v_lshl_add_u64 v[116:117], v[2:3], 0, v[114:115]
	global_load_dwordx4 a[64:67], v[116:117], off
	global_load_dwordx4 a[68:71], v[116:117], off offset:16
	v_add_u32_e32 v114, 0x2000, v112
	v_lshl_add_u64 v[116:117], v[2:3], 0, v[114:115]
	global_load_dwordx4 a[72:75], v[116:117], off
	global_load_dwordx4 a[76:79], v[116:117], off offset:16
	v_add_u32_e32 v114, 0x4000, v112
	v_lshl_add_u64 v[116:117], v[2:3], 0, v[114:115]
	global_load_dwordx4 a[80:83], v[116:117], off
	global_load_dwordx4 a[84:87], v[116:117], off offset:16
	v_add_u32_e32 v114, 0x6000, v112
	v_lshl_add_u64 v[116:117], v[2:3], 0, v[114:115]
	global_load_dwordx4 a[88:91], v[116:117], off
	global_load_dwordx4 a[92:95], v[116:117], off offset:16
	v_mov_b32_e32 v114, v113
	v_lshl_add_u64 v[116:117], v[2:3], 0, v[114:115]
	global_load_dwordx4 a[96:99], v[116:117], off
	global_load_dwordx4 a[100:103], v[116:117], off offset:16
	v_add_u32_e32 v114, 0x2000, v113
	v_lshl_add_u64 v[116:117], v[2:3], 0, v[114:115]
	global_load_dwordx4 a[104:107], v[116:117], off
	global_load_dwordx4 a[108:111], v[116:117], off offset:16
	v_add_u32_e32 v114, 0x4000, v113
	v_lshl_add_u64 v[116:117], v[2:3], 0, v[114:115]
	global_load_dwordx4 a[112:115], v[116:117], off
	global_load_dwordx4 a[116:119], v[116:117], off offset:16
	v_add_u32_e32 v114, 0x6000, v113
	v_lshl_add_u64 v[116:117], v[2:3], 0, v[114:115]
	global_load_dwordx4 a[120:123], v[116:117], off
	global_load_dwordx4 a[124:127], v[116:117], off offset:16
	v_add_u32_e32 v114, 0x8000, v110
	v_lshl_add_u64 v[116:117], v[2:3], 0, v[114:115]
	global_load_dwordx4 a[128:131], v[116:117], off
	global_load_dwordx4 a[132:135], v[116:117], off offset:16
	v_add_u32_e32 v114, 0xa000, v110
	v_lshl_add_u64 v[116:117], v[2:3], 0, v[114:115]
	global_load_dwordx4 a[136:139], v[116:117], off
	global_load_dwordx4 a[140:143], v[116:117], off offset:16
	v_add_u32_e32 v114, 0xc000, v110
	v_lshl_add_u64 v[116:117], v[2:3], 0, v[114:115]
	global_load_dwordx4 a[144:147], v[116:117], off
	global_load_dwordx4 a[148:151], v[116:117], off offset:16
	v_add_u32_e32 v114, 0xe000, v110
	v_lshl_add_u64 v[116:117], v[2:3], 0, v[114:115]
	global_load_dwordx4 a[152:155], v[116:117], off
	global_load_dwordx4 a[156:159], v[116:117], off offset:16
	v_add_u32_e32 v114, 0x8000, v111
	v_lshl_add_u64 v[116:117], v[2:3], 0, v[114:115]
	global_load_dwordx4 a[160:163], v[116:117], off
	global_load_dwordx4 a[164:167], v[116:117], off offset:16
	v_add_u32_e32 v114, 0xa000, v111
	v_lshl_add_u64 v[116:117], v[2:3], 0, v[114:115]
	global_load_dwordx4 a[168:171], v[116:117], off
	global_load_dwordx4 a[172:175], v[116:117], off offset:16
	v_add_u32_e32 v114, 0xc000, v111
	v_lshl_add_u64 v[116:117], v[2:3], 0, v[114:115]
	global_load_dwordx4 a[176:179], v[116:117], off
	global_load_dwordx4 a[180:183], v[116:117], off offset:16
	v_add_u32_e32 v114, 0xe000, v111
	v_lshl_add_u64 v[116:117], v[2:3], 0, v[114:115]
	global_load_dwordx4 a[184:187], v[116:117], off
	global_load_dwordx4 a[188:191], v[116:117], off offset:16
	v_add_u32_e32 v114, 0x8000, v112
	v_lshl_add_u64 v[116:117], v[2:3], 0, v[114:115]
	global_load_dwordx4 a[192:195], v[116:117], off
	global_load_dwordx4 a[196:199], v[116:117], off offset:16
	v_add_u32_e32 v114, 0xa000, v112
	v_lshl_add_u64 v[116:117], v[2:3], 0, v[114:115]
	global_load_dwordx4 a[200:203], v[116:117], off
	global_load_dwordx4 a[204:207], v[116:117], off offset:16
	v_add_u32_e32 v114, 0xc000, v112
	v_lshl_add_u64 v[116:117], v[2:3], 0, v[114:115]
	global_load_dwordx4 a[208:211], v[116:117], off
	global_load_dwordx4 a[212:215], v[116:117], off offset:16
	v_add_u32_e32 v114, 0xe000, v112
	v_lshl_add_u64 v[116:117], v[2:3], 0, v[114:115]
	global_load_dwordx4 a[216:219], v[116:117], off
	global_load_dwordx4 a[220:223], v[116:117], off offset:16
	v_add_u32_e32 v114, 0x8000, v113
	v_lshl_add_u64 v[116:117], v[2:3], 0, v[114:115]
	global_load_dwordx4 a[224:227], v[116:117], off
	global_load_dwordx4 a[228:231], v[116:117], off offset:16
	v_add_u32_e32 v114, 0xa000, v113
	v_lshl_add_u64 v[116:117], v[2:3], 0, v[114:115]
	global_load_dwordx4 a[232:235], v[116:117], off
	global_load_dwordx4 a[236:239], v[116:117], off offset:16
	v_add_u32_e32 v114, 0xc000, v113
	v_lshl_add_u64 v[116:117], v[2:3], 0, v[114:115]
	global_load_dwordx4 a[240:243], v[116:117], off
	global_load_dwordx4 a[244:247], v[116:117], off offset:16
	v_add_u32_e32 v114, 0xe000, v113
	v_lshl_add_u64 v[116:117], v[2:3], 0, v[114:115]
	global_load_dwordx4 a[248:251], v[116:117], off
	global_load_dwordx4 a[252:255], v[116:117], off offset:16
	s_movk_i32 s12, 0x2000
	s_movk_i32 s13, 0x3000
	v_lshlrev_b32_e32 v29, 3, v1
	s_lshl_b32 s18, s24, 5
	s_cmp_lt_u32 s24, 16
	s_cselect_b64 s[22:23], -1, 0
	s_and_b64 s[16:17], s[22:23], exec
	s_movk_i32 s0, 0x800
	s_cselect_b32 s0, s0, 0x1800
	s_mov_b32 s1, 0
	v_bfe_u32 v4, v0, 3, 1
	v_and_b32_e32 v5, 7, v0
	v_or3_b32 v16, s18, v29, v5
	v_lshlrev_b32_e32 v7, 1, v4
	v_lshrrev_b32_e32 v3, 2, v0
	v_bfe_u32 v2, v0, 5, 1
	v_and_b32_e32 v6, 4, v3
	v_or3_b32 v6, v6, v7, v2
	v_mov_b32_e32 v3, v17
	v_lshlrev_b32_e32 v2, 1, v16
	s_waitcnt vmcnt(0)
	ds_read_b32 v27, v17 offset:32772
	s_waitcnt lgkmcnt(0)
	v_lshl_or_b32 v18, v27, 3, v6
	v_ashrrev_i32_e32 v19, 31, v18
	v_lshlrev_b64 v[8:9], 20, v[18:19]
	v_lshl_add_u64 v[10:11], s[4:5], 0, v[8:9]
	v_lshl_add_u64 v[20:21], v[10:11], 0, v[2:3]
	v_add_co_u32_e32 v24, vcc, s3, v20
	v_lshl_add_u64 v[8:9], s[6:7], 0, v[8:9]
	s_nop 0
	v_addc_co_u32_e32 v25, vcc, 0, v21, vcc
	v_add_co_u32_e32 v12, vcc, s12, v20
	v_lshl_add_u64 v[2:3], v[8:9], 0, v[2:3]
	s_nop 0
	v_addc_co_u32_e32 v13, vcc, 0, v21, vcc
	v_add_co_u32_e32 v30, vcc, s13, v20
	v_lshl_add_u64 v[22:23], v[2:3], 0, s[0:1]
	s_nop 0
	v_addc_co_u32_e32 v31, vcc, 0, v21, vcc
	v_add_co_u32_e32 v2, vcc, 0x2000, v22
	global_load_ushort v8, v[20:21], off
	global_load_ushort v9, v[20:21], off offset:2048
	global_load_ushort v11, v[12:13], off offset:-4096
	global_load_ushort v10, v[12:13], off
	s_nop 0
	global_load_ushort v12, v[12:13], off offset:2048
	v_addc_co_u32_e32 v3, vcc, 0, v23, vcc
	global_load_ushort v14, v[22:23], off
	s_nop 0
	global_load_ushort v24, v[24:25], off offset:2048
	s_nop 0
	global_load_ushort v13, v[30:31], off
	global_load_ushort v15, v[30:31], off offset:2048
	global_load_ushort v25, v[2:3], off
	v_cmp_gt_u32_e32 vcc, 64, v0
	s_and_saveexec_b64 s[12:13], vcc
	s_cbranch_execz .LBB2_9
	v_lshlrev_b32_e32 v2, 2, v5
	v_mov_b32_e32 v3, v17
	v_lshl_add_u64 v[2:3], s[10:11], 0, v[2:3]

.LBB2_9:
	s_or_b64 exec, exec, s[12:13]
	v_mov_b32_e32 v26, 0
	s_waitcnt lgkmcnt(0)
	s_barrier
	ds_read_b32 v31, v26 offset:32768
	v_bfe_u32 v7, v0, 4, 2
	v_lshlrev_b32_e32 v30, 1, v1
	v_lshlrev_b64 v[2:3], 19, v[18:19]
	s_mov_b32 s13, 0
	s_waitcnt lgkmcnt(0)
	v_cmp_ne_u32_e64 s[0:1], 0, v31
	s_and_b64 vcc, exec, s[0:1]
	s_cbranch_vccnz .LBB2_11
	s_and_b32 s3, s2, 7
	s_lshr_b32 s24, s2, 3
	s_lshl_b32 s12, s24, 5
	s_lshl_b32 s16, s3, 23
	s_cmpk_lt_u32 s2, 0x80
	s_cselect_b64 s[22:23], -1, 0
	s_movk_i32 s17, 0x800
	s_and_b64 s[10:11], s[22:23], exec
	s_cselect_b32 s10, s17, 0x1800
	s_and_b32 s2, s2, 0x3ffff8
	v_or_b32_e32 v2, s2, v30
	v_lshl_or_b32 v2, v2, 10, v28
	v_ashrrev_i32_e32 v3, 31, v2
	s_waitcnt vmcnt(8)
	v_mov_b32_e32 v19, 0
	v_or3_b32 v16, s12, v29, v5
	v_lshl_or_b32 v18, v6, 20, s16
	v_mov_b32_e32 v9, v19
	s_waitcnt vmcnt(8)
	v_lshl_add_u64 v[10:11], s[4:5], 0, v[18:19]
	v_lshlrev_b32_e32 v8, 1, v16
	s_movk_i32 s2, 0x1000
	v_lshl_add_u64 v[20:21], v[10:11], 0, v[8:9]
	v_add_co_u32_e32 v28, vcc, s2, v20
	s_movk_i32 s17, 0x2000
	s_nop 0
	v_addc_co_u32_e32 v29, vcc, 0, v21, vcc
	v_add_co_u32_e32 v30, vcc, s17, v20
	s_movk_i32 s18, 0x3000
	s_waitcnt vmcnt(4)
	v_lshl_add_u64 v[12:13], s[6:7], 0, v[18:19]
	v_addc_co_u32_e32 v31, vcc, 0, v21, vcc
	s_mov_b32 s11, 0
	v_lshl_add_u64 v[22:23], v[12:13], 0, v[8:9]
	v_add_co_u32_e32 v32, vcc, s18, v20
	v_lshl_add_u64 v[22:23], v[22:23], 0, s[10:11]
	s_nop 0
	v_addc_co_u32_e32 v33, vcc, 0, v21, vcc
	global_load_ushort v8, v[20:21], off
	global_load_ushort v9, v[20:21], off offset:2048
	global_load_ushort v11, v[30:31], off offset:-4096
	global_load_ushort v10, v[30:31], off
	global_load_ushort v12, v[30:31], off offset:2048
	global_load_ushort v24, v[28:29], off offset:2048
	global_load_ushort v13, v[32:33], off
	global_load_ushort v15, v[32:33], off offset:2048
	v_add_co_u32_e32 v28, vcc, s17, v22
	global_load_ushort v14, v[22:23], off
	s_nop 0
	v_addc_co_u32_e32 v29, vcc, 0, v23, vcc
	global_load_ushort v25, v[28:29], off
	v_lshl_or_b32 v18, s3, 3, v6
	v_mov_b32_e32 v17, v19
	v_mov_b32_e32 v27, s3
	s_waitcnt vmcnt(10)
	s_waitcnt vmcnt(0)
	s_waitcnt vmcnt(0)
	s_waitcnt vmcnt(0)
	s_waitcnt vmcnt(0)
	s_waitcnt vmcnt(0)
	s_waitcnt vmcnt(0)
	s_waitcnt vmcnt(0)
	s_waitcnt vmcnt(0)
	s_waitcnt vmcnt(0)
	s_waitcnt vmcnt(0)
	s_waitcnt vmcnt(0)
	s_waitcnt vmcnt(0)
	s_waitcnt vmcnt(0)
	s_waitcnt vmcnt(0)
	s_waitcnt vmcnt(0)
	s_waitcnt vmcnt(0)
	s_waitcnt vmcnt(0)
	s_waitcnt vmcnt(0)
	s_waitcnt vmcnt(0)
	s_waitcnt vmcnt(0)
	s_waitcnt vmcnt(0)
	s_waitcnt vmcnt(0)
	s_waitcnt vmcnt(0)
	s_waitcnt vmcnt(0)
	s_waitcnt vmcnt(0)
	s_waitcnt vmcnt(0)
	s_waitcnt vmcnt(0)
	s_waitcnt vmcnt(0)
	s_waitcnt vmcnt(0)
	s_waitcnt vmcnt(0)
	v_lshlrev_b64 v[118:119], 5, v[2:3]
	v_lshl_add_u64 v[118:119], s[14:15], 0, v[118:119]
	v_mov_b32_e32 v115, 0
	v_lshlrev_b32_e32 v110, 11, v1
	v_add_u32_e32 v111, 1, v1
	v_and_b32_e32 v111, 3, v111
	v_lshlrev_b32_e32 v111, 11, v111
	v_add_u32_e32 v112, 2, v1
	v_and_b32_e32 v112, 3, v112
	v_lshlrev_b32_e32 v112, 11, v112
	v_add_u32_e32 v113, 3, v1
	v_and_b32_e32 v113, 3, v113
	v_lshlrev_b32_e32 v113, 11, v113
	v_mov_b32_e32 v114, v110
	v_lshl_add_u64 v[116:117], v[118:119], 0, v[114:115]
	global_load_dwordx4 a[0:3], v[116:117], off
	global_load_dwordx4 a[4:7], v[116:117], off offset:16
	v_add_u32_e32 v114, 0x2000, v110
	v_lshl_add_u64 v[116:117], v[118:119], 0, v[114:115]
	global_load_dwordx4 a[8:11], v[116:117], off
	global_load_dwordx4 a[12:15], v[116:117], off offset:16
	v_add_u32_e32 v114, 0x4000, v110
	v_lshl_add_u64 v[116:117], v[118:119], 0, v[114:115]
	global_load_dwordx4 a[16:19], v[116:117], off
	global_load_dwordx4 a[20:23], v[116:117], off offset:16
	v_add_u32_e32 v114, 0x6000, v110
	v_lshl_add_u64 v[116:117], v[118:119], 0, v[114:115]
	global_load_dwordx4 a[24:27], v[116:117], off
	global_load_dwordx4 a[28:31], v[116:117], off offset:16
	v_mov_b32_e32 v114, v111
	v_lshl_add_u64 v[116:117], v[118:119], 0, v[114:115]
	global_load_dwordx4 a[32:35], v[116:117], off
	global_load_dwordx4 a[36:39], v[116:117], off offset:16
	v_add_u32_e32 v114, 0x2000, v111
	v_lshl_add_u64 v[116:117], v[118:119], 0, v[114:115]
	global_load_dwordx4 a[40:43], v[116:117], off
	global_load_dwordx4 a[44:47], v[116:117], off offset:16
	v_add_u32_e32 v114, 0x4000, v111
	v_lshl_add_u64 v[116:117], v[118:119], 0, v[114:115]
	global_load_dwordx4 a[48:51], v[116:117], off
	global_load_dwordx4 a[52:55], v[116:117], off offset:16
	v_add_u32_e32 v114, 0x6000, v111
	v_lshl_add_u64 v[116:117], v[118:119], 0, v[114:115]
	global_load_dwordx4 a[56:59], v[116:117], off
	global_load_dwordx4 a[60:63], v[116:117], off offset:16
	v_mov_b32_e32 v114, v112
	v_lshl_add_u64 v[116:117], v[118:119], 0, v[114:115]
	global_load_dwordx4 a[64:67], v[116:117], off
	global_load_dwordx4 a[68:71], v[116:117], off offset:16
	v_add_u32_e32 v114, 0x2000, v112
	v_lshl_add_u64 v[116:117], v[118:119], 0, v[114:115]
	global_load_dwordx4 a[72:75], v[116:117], off
	global_load_dwordx4 a[76:79], v[116:117], off offset:16
	v_add_u32_e32 v114, 0x4000, v112
	v_lshl_add_u64 v[116:117], v[118:119], 0, v[114:115]
	global_load_dwordx4 a[80:83], v[116:117], off
	global_load_dwordx4 a[84:87], v[116:117], off offset:16
	v_add_u32_e32 v114, 0x6000, v112
	v_lshl_add_u64 v[116:117], v[118:119], 0, v[114:115]
	global_load_dwordx4 a[88:91], v[116:117], off
	global_load_dwordx4 a[92:95], v[116:117], off offset:16
	v_mov_b32_e32 v114, v113
	v_lshl_add_u64 v[116:117], v[118:119], 0, v[114:115]
	global_load_dwordx4 a[96:99], v[116:117], off
	global_load_dwordx4 a[100:103], v[116:117], off offset:16
	v_add_u32_e32 v114, 0x2000, v113
	v_lshl_add_u64 v[116:117], v[118:119], 0, v[114:115]
	global_load_dwordx4 a[104:107], v[116:117], off
	global_load_dwordx4 a[108:111], v[116:117], off offset:16
	v_add_u32_e32 v114, 0x4000, v113
	v_lshl_add_u64 v[116:117], v[118:119], 0, v[114:115]
	global_load_dwordx4 a[112:115], v[116:117], off
	global_load_dwordx4 a[116:119], v[116:117], off offset:16
	v_add_u32_e32 v114, 0x6000, v113
	v_lshl_add_u64 v[116:117], v[118:119], 0, v[114:115]
	global_load_dwordx4 a[120:123], v[116:117], off
	global_load_dwordx4 a[124:127], v[116:117], off offset:16
	v_add_u32_e32 v114, 0x8000, v110
	v_lshl_add_u64 v[116:117], v[118:119], 0, v[114:115]
	global_load_dwordx4 a[128:131], v[116:117], off
	global_load_dwordx4 a[132:135], v[116:117], off offset:16
	v_add_u32_e32 v114, 0xa000, v110
	v_lshl_add_u64 v[116:117], v[118:119], 0, v[114:115]
	global_load_dwordx4 a[136:139], v[116:117], off
	global_load_dwordx4 a[140:143], v[116:117], off offset:16
	v_add_u32_e32 v114, 0xc000, v110
	v_lshl_add_u64 v[116:117], v[118:119], 0, v[114:115]
	global_load_dwordx4 a[144:147], v[116:117], off
	global_load_dwordx4 a[148:151], v[116:117], off offset:16
	v_add_u32_e32 v114, 0xe000, v110
	v_lshl_add_u64 v[116:117], v[118:119], 0, v[114:115]
	global_load_dwordx4 a[152:155], v[116:117], off
	global_load_dwordx4 a[156:159], v[116:117], off offset:16
	v_add_u32_e32 v114, 0x8000, v111
	v_lshl_add_u64 v[116:117], v[118:119], 0, v[114:115]
	global_load_dwordx4 a[160:163], v[116:117], off
	global_load_dwordx4 a[164:167], v[116:117], off offset:16
	v_add_u32_e32 v114, 0xa000, v111
	v_lshl_add_u64 v[116:117], v[118:119], 0, v[114:115]
	global_load_dwordx4 a[168:171], v[116:117], off
	global_load_dwordx4 a[172:175], v[116:117], off offset:16
	v_add_u32_e32 v114, 0xc000, v111
	v_lshl_add_u64 v[116:117], v[118:119], 0, v[114:115]
	global_load_dwordx4 a[176:179], v[116:117], off
	global_load_dwordx4 a[180:183], v[116:117], off offset:16
	v_add_u32_e32 v114, 0xe000, v111
	v_lshl_add_u64 v[116:117], v[118:119], 0, v[114:115]
	global_load_dwordx4 a[184:187], v[116:117], off
	global_load_dwordx4 a[188:191], v[116:117], off offset:16
	v_add_u32_e32 v114, 0x8000, v112
	v_lshl_add_u64 v[116:117], v[118:119], 0, v[114:115]
	global_load_dwordx4 a[192:195], v[116:117], off
	global_load_dwordx4 a[196:199], v[116:117], off offset:16
	v_add_u32_e32 v114, 0xa000, v112
	v_lshl_add_u64 v[116:117], v[118:119], 0, v[114:115]
	global_load_dwordx4 a[200:203], v[116:117], off
	global_load_dwordx4 a[204:207], v[116:117], off offset:16
	v_add_u32_e32 v114, 0xc000, v112
	v_lshl_add_u64 v[116:117], v[118:119], 0, v[114:115]
	global_load_dwordx4 a[208:211], v[116:117], off
	global_load_dwordx4 a[212:215], v[116:117], off offset:16
	v_add_u32_e32 v114, 0xe000, v112
	v_lshl_add_u64 v[116:117], v[118:119], 0, v[114:115]
	global_load_dwordx4 a[216:219], v[116:117], off
	global_load_dwordx4 a[220:223], v[116:117], off offset:16
	v_add_u32_e32 v114, 0x8000, v113
	v_lshl_add_u64 v[116:117], v[118:119], 0, v[114:115]
	global_load_dwordx4 a[224:227], v[116:117], off
	global_load_dwordx4 a[228:231], v[116:117], off offset:16
	v_add_u32_e32 v114, 0xa000, v113
	v_lshl_add_u64 v[116:117], v[118:119], 0, v[114:115]
	global_load_dwordx4 a[232:235], v[116:117], off
	global_load_dwordx4 a[236:239], v[116:117], off offset:16
	v_add_u32_e32 v114, 0xc000, v113
	v_lshl_add_u64 v[116:117], v[118:119], 0, v[114:115]
	global_load_dwordx4 a[240:243], v[116:117], off
	global_load_dwordx4 a[244:247], v[116:117], off offset:16
	v_add_u32_e32 v114, 0xe000, v113
	v_lshl_add_u64 v[116:117], v[118:119], 0, v[114:115]
	global_load_dwordx4 a[248:251], v[116:117], off
	global_load_dwordx4 a[252:255], v[116:117], off offset:16
	v_mov_b32_e32 v3, v19
	v_lshlrev_b32_e32 v2, 19, v18
	s_waitcnt vmcnt(0)
.LBB2_11:
	v_and_b32_e32 v28, 8, v0
	v_lshlrev_b32_e32 v0, 1, v5
	v_lshl_or_b32 v38, v6, 4, v0
	v_lshlrev_b32_e32 v0, 7, v1
	v_mov_b32_e32 v29, 0xeeeeeeee
	v_mov_b32_e32 v30, 0x44444444
	v_cmp_eq_u32_e32 vcc, 0, v28
	v_lshl_add_u64 v[2:3], s[20:21], 0, v[2:3]
	v_lshl_or_b32 v40, s24, 9, v0
	v_cndmask_b32_e64 v0, 0, 1, s[0:1]
	v_cndmask_b32_e32 v28, v29, v30, vcc
	s_waitcnt vmcnt(9)
	v_and_b32_e32 v44, 0xffff, v8
	s_waitcnt vmcnt(8)
	v_and_b32_e32 v43, 0xffff, v9
	s_waitcnt vmcnt(7)
	v_and_b32_e32 v42, 0xffff, v11
	s_waitcnt vmcnt(3)
	v_and_b32_e32 v41, 0xffff, v24
	v_and_b32_e32 v29, 0xffff, v10
	v_and_b32_e32 v30, 0xffff, v12
	s_waitcnt vmcnt(2)
	v_and_b32_e32 v31, 0xffff, v13
	s_waitcnt vmcnt(1)
	v_and_b32_e32 v32, 0xffff, v15
	v_and_b32_e32 v45, 0xffff, v14
	s_waitcnt vmcnt(0)
	v_and_b32_e32 v33, 0xffff, v25
	s_mov_b32 s19, 0x20000
	s_mov_b32 s18, 0x40000
	s_and_b32 s17, s9, 0xffff
	s_mov_b32 s16, s8
	v_lshl_add_u64 v[24:25], v[16:17], 2, v[2:3]
	v_lshlrev_b32_e32 v35, 9, v4
	v_lshlrev_b32_e32 v36, 7, v7
	v_lshlrev_b32_e32 v37, 4, v5
	v_cmp_eq_u32_e64 s[2:3], 0, v4
	v_lshl_add_u32 v34, v1, 10, v35
	v_add3_u32 v34, v34, v36, v37
	v_add_u32_e32 v121, 1, v1
	v_add_u32_e32 v122, 2, v1
	v_add_u32_e32 v123, 3, v1
	v_and_b32_e32 v121, 3, v121
	v_and_b32_e32 v122, 3, v122
	v_and_b32_e32 v123, 3, v123
	v_lshl_add_u32 v121, v121, 10, v35
	v_lshl_add_u32 v122, v122, 10, v35
	v_lshl_add_u32 v123, v123, 10, v35
	v_add3_u32 v121, v121, v36, v37
	v_add3_u32 v122, v122, v36, v37
	v_add3_u32 v123, v123, v36, v37
	v_lshl_or_b32 v39, v27, 14, v34
	s_mov_b64 s[6:7], 0
	s_mov_b32 s28, 0x10000
	v_cmp_ne_u32_e64 s[0:1], 1, v0
	v_mov_b32_e32 v46, 0
	s_mov_b32 s29, 0
	v_lshl_add_u32 v120, v27, 14, v40
	v_or_b32_e32 v120, v120, v38
	s_mov_b32 s37, 0
	s_cmp_eq_u32 s29, 0
	s_cbranch_scc1 .LBB2_23
.LBB2_12:
	s_add_i32 s12, s29, -1
	s_and_b32 s30, s12, 1
	s_bitcmp1_b32 s12, 1
	s_cselect_b32 s4, 0x10001, 0
	v_lshl_add_u32 v47, s30, 17, v39
	s_lshl_b32 s31, s30, 14
	s_lshl_b64 s[10:11], s[12:13], 12
	v_add_u32_e32 v48, 0x1000, v47
	v_add_u32_e32 v49, 0x2000, v47
	v_add_u32_e32 v50, 0x3000, v47
	v_or_b32_e32 v110, s31, v34
	v_add_u32_e32 v111, s31, v121
	v_lshl_add_u64 v[112:113], v[24:25], 0, s[10:11]
	v_add_u32_e32 v124, s31, v122
	v_add_u32_e32 v125, s31, v123
	s_lshl_b32 s32, s29, 13
	s_add_i32 s32, s32, 0x2000
	s_mov_b32 s33, 0
	v_lshl_add_u64 v[114:115], v[20:21], 0, s[32:33]
	v_lshl_add_u64 v[118:119], v[22:23], 0, s[32:33]
	v_add_co_u32_e32 v116, vcc, 0x1000, v114
	v_mov_b64_e32 v[62:63], 0
	v_mov_b64_e32 v[64:65], 0
	v_addc_co_u32_e32 v117, vcc, 0, v115, vcc
	v_mov_b64_e32 v[66:67], 0
	v_mov_b64_e32 v[68:69], 0
	s_mov_b32 s31, 0
	s_sleep 1
.Lrec_poll:
	buffer_load_dwordx4 v[0:3], v47, s[16:19], 0 offen sc1
	buffer_load_dwordx4 v[4:7], v48, s[16:19], 0 offen sc1
	buffer_load_dwordx4 v[8:11], v49, s[16:19], 0 offen sc1
	buffer_load_dwordx4 v[12:15], v50, s[16:19], 0 offen sc1
	s_cmp_eq_u32 s4, 0
	s_cbranch_scc1 .Lrec_poll_or
	s_waitcnt vmcnt(3)
	ds_write_b128 v110, v[0:3]
	v_and_b32_e32 v52, v0, v1
	v_bitop3_b32 v52, v52, v3, v2 bitop3:0x80
	s_waitcnt vmcnt(2)
	ds_write_b128 v110, v[4:7] offset:4096
	v_bitop3_b32 v52, v4, v5, v52 bitop3:0x80
	v_bitop3_b32 v52, v52, v7, v6 bitop3:0x80
	s_waitcnt vmcnt(1)
	ds_write_b128 v110, v[8:11] offset:8192
	v_bitop3_b32 v52, v8, v9, v52 bitop3:0x80
	v_bitop3_b32 v52, v52, v11, v10 bitop3:0x80
	s_waitcnt vmcnt(0)
	ds_write_b128 v110, v[12:15] offset:12288
	v_bitop3_b32 v52, v12, v13, v52 bitop3:0x80
	v_bitop3_b32 v52, v52, v15, v14 bitop3:0x80
	s_branch .Lrec_poll_chk
.Lrec_poll_or:
	s_waitcnt vmcnt(3)
	ds_write_b128 v110, v[0:3]
	v_or_b32_e32 v52, v0, v1
	v_or3_b32 v52, v52, v2, v3
	s_waitcnt vmcnt(2)
	ds_write_b128 v110, v[4:7] offset:4096
	v_or3_b32 v52, v4, v52, v5
	v_or3_b32 v52, v52, v6, v7
	s_waitcnt vmcnt(1)
	ds_write_b128 v110, v[8:11] offset:8192
	v_or3_b32 v52, v8, v52, v9
	v_or3_b32 v52, v52, v10, v11
	s_waitcnt vmcnt(0)
	ds_write_b128 v110, v[12:15] offset:12288
	v_or3_b32 v52, v12, v52, v13
	v_or3_b32 v52, v52, v14, v15

.LBB2_20:
	s_mov_b64 exec, -1
	s_cmpk_eq_i32 s29, 0x7f
	s_waitcnt lgkmcnt(0)
	s_barrier
	ds_read_b128 v[50:53], v111
	ds_read_b128 v[54:57], v111 offset:4096
	ds_read_b128 v[58:61], v111 offset:8192
	global_store_dword v[112:113], v46, off
	ds_read_b128 v[46:49], v111 offset:12288
	ds_read_b128 v[78:81], v124
	ds_read_b128 v[82:85], v124 offset:4096
	ds_read_b128 v[86:89], v124 offset:8192
	ds_read_b128 v[90:93], v124 offset:12288
	ds_read_b128 v[94:97], v125
	ds_read_b128 v[98:101], v125 offset:4096
	ds_read_b128 v[102:105], v125 offset:8192
	ds_read_b128 v[106:109], v125 offset:12288
	s_cbranch_scc1 .Lrec_nopf
	global_load_ushort v29, v[114:115], off
	global_load_ushort v30, v[114:115], off offset:2048
	global_load_ushort v31, v[116:117], off
	global_load_ushort v32, v[116:117], off offset:2048
	global_load_ushort v33, v[118:119], off
.Lrec_nopf:
	v_cvt_f32_f16_e32 v112, v44
	v_cvt_f32_f16_e32 v113, v43
	v_cvt_f32_f16_e32 v114, v42
	v_cvt_f32_f16_e32 v115, v41
	v_cvt_f32_f16_e32 v118, v45
	v_cndmask_b32_e64 v116, 0, v118, s[22:23]
	v_cndmask_b32_e64 v117, v118, 0, s[22:23]
	v_smfmac_f32_16x16x64_f16 v[62:65], v[0:3], a[0:7], v28
	v_smfmac_f32_16x16x64_f16 v[66:69], v[0:3], a[128:135], v28
	v_smfmac_f32_16x16x64_f16 v[62:65], v[4:7], a[8:15], v28
	v_smfmac_f32_16x16x64_f16 v[66:69], v[4:7], a[136:143], v28
	v_smfmac_f32_16x16x64_f16 v[62:65], v[8:11], a[16:23], v28
	v_smfmac_f32_16x16x64_f16 v[66:69], v[8:11], a[144:151], v28
	v_smfmac_f32_16x16x64_f16 v[62:65], v[12:15], a[24:31], v28
	v_smfmac_f32_16x16x64_f16 v[66:69], v[12:15], a[152:159], v28
	s_waitcnt lgkmcnt(11)
	v_smfmac_f32_16x16x64_f16 v[62:65], v[50:53], a[32:39], v28
	v_smfmac_f32_16x16x64_f16 v[66:69], v[50:53], a[160:167], v28
	s_waitcnt lgkmcnt(10)
	v_smfmac_f32_16x16x64_f16 v[62:65], v[54:57], a[40:47], v28
	v_smfmac_f32_16x16x64_f16 v[66:69], v[54:57], a[168:175], v28
	s_waitcnt lgkmcnt(9)
	v_smfmac_f32_16x16x64_f16 v[62:65], v[58:61], a[48:55], v28
	v_smfmac_f32_16x16x64_f16 v[66:69], v[58:61], a[176:183], v28
	s_waitcnt lgkmcnt(8)
	v_smfmac_f32_16x16x64_f16 v[62:65], v[46:49], a[56:63], v28
	v_smfmac_f32_16x16x64_f16 v[66:69], v[46:49], a[184:191], v28
	s_waitcnt lgkmcnt(7)
	v_smfmac_f32_16x16x64_f16 v[62:65], v[78:81], a[64:71], v28
	v_smfmac_f32_16x16x64_f16 v[66:69], v[78:81], a[192:199], v28
	s_waitcnt lgkmcnt(6)
	v_smfmac_f32_16x16x64_f16 v[62:65], v[82:85], a[72:79], v28
	v_smfmac_f32_16x16x64_f16 v[66:69], v[82:85], a[200:207], v28
	s_waitcnt lgkmcnt(5)
	v_smfmac_f32_16x16x64_f16 v[62:65], v[86:89], a[80:87], v28
	v_smfmac_f32_16x16x64_f16 v[66:69], v[86:89], a[208:215], v28
	s_waitcnt lgkmcnt(4)
	v_smfmac_f32_16x16x64_f16 v[62:65], v[90:93], a[88:95], v28
	v_smfmac_f32_16x16x64_f16 v[66:69], v[90:93], a[216:223], v28
	s_waitcnt lgkmcnt(3)
	v_smfmac_f32_16x16x64_f16 v[62:65], v[94:97], a[96:103], v28
	v_smfmac_f32_16x16x64_f16 v[66:69], v[94:97], a[224:231], v28
	s_waitcnt lgkmcnt(2)
	v_smfmac_f32_16x16x64_f16 v[62:65], v[98:101], a[104:111], v28
	v_smfmac_f32_16x16x64_f16 v[66:69], v[98:101], a[232:239], v28
	s_waitcnt lgkmcnt(1)
	v_smfmac_f32_16x16x64_f16 v[62:65], v[102:105], a[112:119], v28
	v_smfmac_f32_16x16x64_f16 v[66:69], v[102:105], a[240:247], v28
	s_waitcnt lgkmcnt(0)
	v_smfmac_f32_16x16x64_f16 v[62:65], v[106:109], a[120:127], v28
	v_smfmac_f32_16x16x64_f16 v[66:69], v[106:109], a[248:255], v28
	s_nop 6
	s_waitcnt vmcnt(0)
	v_permlane32_swap_b32_e32 v62, v63
	v_permlane32_swap_b32_e32 v64, v65
	v_permlane32_swap_b32_e32 v66, v67
	v_permlane32_swap_b32_e32 v68, v69
	v_add_f32_e32 v2, v62, v63
	v_add_f32_e32 v0, v64, v65
	v_add_f32_e32 v1, v66, v67
	v_add_f32_e32 v3, v68, v69
	s_branch .Lrec_gate2
.LBB2_23:
	v_mov_b32_e32 v0, 0
	v_mov_b32_e32 v1, 0
	v_mov_b32_e32 v2, 0
	v_mov_b32_e32 v3, 0
	v_cvt_f32_f16_e32 v112, v44
	v_cvt_f32_f16_e32 v113, v43
	v_cvt_f32_f16_e32 v114, v42
	v_cvt_f32_f16_e32 v115, v41
	v_cvt_f32_f16_e32 v118, v45
	v_cndmask_b32_e64 v116, 0, v118, s[22:23]
	v_cndmask_b32_e64 v117, v118, 0, s[22:23]
.Lrec_gate2:
	v_cndmask_b32_e64 v4, v2, v0, s[2:3]
	v_mov_b32_e32 v6, 0
	v_cndmask_b32_e64 v5, v1, v3, s[2:3]
	v_mov_b32_e32 v7, 0
	v_mov_b32_dpp v6, v4 row_ror:8 row_mask:0xf bank_mask:0xf
	s_nop 0
	v_mov_b32_dpp v7, v5 row_ror:8 row_mask:0xf bank_mask:0xf
	v_cndmask_b32_e64 v0, v0, v6, s[2:3]
	v_cndmask_b32_e64 v2, v6, v2, s[2:3]
	v_cndmask_b32_e64 v1, v7, v1, s[2:3]
	v_cndmask_b32_e64 v3, v3, v7, s[2:3]
	v_add_f32_e32 v2, v2, v112
	v_add_f32_e32 v0, v0, v113
	v_add_f32_e32 v1, v1, v114
	v_add_f32_e32 v3, v3, v115
	v_add_f32_e32 v0, v116, v0
	v_add_f32_e32 v3, v117, v3
	v_mul_f32_e32 v2, 0xbfb8aa3b, v2
	v_mul_f32_e32 v1, 0x4038aa3b, v1
	v_mul_f32_e32 v0, 0xbfb8aa3b, v0
	v_exp_f32_e32 v1, v1
	v_exp_f32_e32 v2, v2
	v_exp_f32_e32 v0, v0
	v_mul_f32_e32 v3, 0xbfb8aa3b, v3
	v_add_f32_e32 v1, 1.0, v1
	v_add_f32_e32 v2, 1.0, v2
	v_exp_f32_e32 v3, v3
	v_rcp_f32_e32 v1, v1
	v_add_f32_e32 v0, 1.0, v0
	v_rcp_f32_e32 v2, v2
	v_rcp_f32_e32 v5, v0
	v_add_f32_e32 v3, 1.0, v3
	v_fma_f32 v0, v1, -2.0, 1.0
	v_mul_f32_e32 v0, v2, v0
	v_rcp_f32_e32 v3, v3
	v_fmac_f32_e32 v0, v26, v5
	v_mul_f32_e32 v1, 0x4038aa3b, v0
	v_exp_f32_e32 v1, v1
	s_cmpk_eq_i32 s29, 0x7f
	s_nop 0
	v_add_f32_e32 v1, 1.0, v1
	v_rcp_f32_e32 v1, v1
	s_nop 0
	v_fma_f32 v1, v1, -2.0, 1.0
	v_mul_f32_e32 v46, v3, v1
	s_cbranch_scc1 .LBB2_29
	v_cvt_f16_f32_e32 v2, v46
	s_cmp_lg_u64 s[0:1], 0
	v_bitop3_b16 v2, s37, v2, -2 bitop3:0xf8
	s_cbranch_scc1 .Lrec_pub_slow
	global_store_short v120, v2, s[8:9]
	s_branch .LBB2_29
